# barriers: agent-scope (sc1) L2 writeback and invalidate instead of system scope; XCD-local leaders release without waiting for their own invalidate
# baseline (speedup 1.0000x reference)
; __device__ __forceinline__ unsigned xb_add(unsigned* p, unsigned v) { return __hip_atomic_fetch_add(p, v, __ATOMIC_RELAXED, __HIP_MEMORY_SCOPE_AGENT); }
; __device__ __forceinline__ void xcd_barrier(const XcdBarrier& b) {
;     ...
;         __builtin_amdgcn_s_waitcnt(0);
;         unsigned nloc = b.st[0], nx = b.st[1];
;         if (nloc == 0u) { xcd_barrier_complete(bar, b.x, nloc, nx); b.st[0] = nloc; b.st[1] = nx; }
;         const unsigned old = xb_add(&bar[XB_XSUB(b.x)], 1u);
;         const unsigned gen = old / nloc;
.LBB0_315:
	s_mov_b64 s[4:5], exec
	v_mbcnt_lo_u32_b32 v0, s4, 0
	s_add_u32 s22, s2, 0x4000
	v_readlane_b32 s6, v255, 7
	v_mbcnt_hi_u32_b32 v2, s5, v0
	s_addc_u32 s23, s3, 0
	s_lshl_b32 s24, s6, 6
	s_mov_b32 s9, 0
	v_cmp_eq_u32_e32 vcc, 0, v2
	s_and_saveexec_b64 s[6:7], vcc
	s_cbranch_execz .LBB0_317
	s_add_i32 s8, s24, 0x500
	s_lshl_b64 s[8:9], s[8:9], 2
	s_add_u32 s8, s22, s8
	s_addc_u32 s9, s23, s9
	s_bcnt1_i32_b64 s4, s[4:5]
	v_mov_b32_e32 v0, 0
	v_mov_b32_e32 v4, s4
	global_atomic_add v4, v0, v4, s[8:9] sc0
	buffer_inv sc1

; __device__ __forceinline__ unsigned xb_add(unsigned* p, unsigned v) { return __hip_atomic_fetch_add(p, v, __ATOMIC_RELAXED, __HIP_MEMORY_SCOPE_AGENT); }
; __device__ __forceinline__ void xcd_barrier(const XcdBarrier& b) {
;     ...
;         if (old + 1u == (gen + 1u) * nloc) {
;             __builtin_amdgcn_fence(__ATOMIC_RELEASE, XB_SCOPE);
;             asm volatile("s_waitcnt vmcnt(0)" ::: "memory");
;             const unsigned og = xb_add(&bar[XB_TOP], 1u);
.LBB0_331:
	s_andn2_saveexec_b64 s[4:5], s[4:5]
	s_cbranch_execz .LBB0_351
	s_mov_b64 s[4:5], exec
	buffer_wbl2 sc1
	s_waitcnt lgkmcnt(0)
	s_waitcnt vmcnt(0)
	v_mbcnt_lo_u32_b32 v0, s4, 0
	v_mbcnt_hi_u32_b32 v2, s5, v0
	v_cmp_eq_u32_e32 vcc, 0, v2
	s_and_saveexec_b64 s[6:7], vcc
	s_cbranch_execz .LBB0_334
	s_bcnt1_i32_b64 s4, s[4:5]
	v_mov_b32_e32 v0, 0x7000
	v_mov_b32_e32 v3, s4
	global_atomic_add v3, v0, v3, s[2:3] offset:1024 sc0

; __device__ __forceinline__ unsigned xb_add(unsigned* p, unsigned v) { return __hip_atomic_fetch_add(p, v, __ATOMIC_RELAXED, __HIP_MEMORY_SCOPE_AGENT); }
; __device__ __forceinline__ void xcd_barrier(const XcdBarrier& b) {
;     ...
;         __builtin_amdgcn_s_waitcnt(0);
;         unsigned nloc = b.st[0], nx = b.st[1];
;         if (nloc == 0u) { xcd_barrier_complete(bar, b.x, nloc, nx); b.st[0] = nloc; b.st[1] = nx; }
;         const unsigned old = xb_add(&bar[XB_XSUB(b.x)], 1u);
;         const unsigned gen = old / nloc;
.LBB0_412:
	s_mov_b64 s[6:7], exec
	v_mbcnt_lo_u32_b32 v0, s6, 0
	s_add_u32 s24, s4, 0x4000
	v_readlane_b32 s8, v255, 7
	v_mbcnt_hi_u32_b32 v1, s7, v0
	s_addc_u32 s25, s5, 0
	s_lshl_b32 s26, s8, 6
	v_cmp_eq_u32_e32 vcc, 0, v1
	s_and_saveexec_b64 s[8:9], vcc
	s_cbranch_execz .LBB0_414
	s_add_i32 s52, s26, 0x500
	s_lshl_b64 s[10:11], s[52:53], 2
	s_add_u32 s10, s24, s10
	s_addc_u32 s11, s25, s11
	s_bcnt1_i32_b64 s6, s[6:7]
	v_mov_b32_e32 v0, s6
	global_atomic_add v5, v3, v0, s[10:11] sc0
	buffer_inv sc1

; __device__ __forceinline__ unsigned xb_ld(unsigned* p)              { return __hip_atomic_load(p, __ATOMIC_RELAXED, __HIP_MEMORY_SCOPE_AGENT); }
; __device__ __forceinline__ unsigned xb_add(unsigned* p, unsigned v) { return __hip_atomic_fetch_add(p, v, __ATOMIC_RELAXED, __HIP_MEMORY_SCOPE_AGENT); }
; #define XB_SPIN(cond, bar) do { unsigned _sp = 0; while (cond) { __builtin_amdgcn_s_sleep(1); \
;     if ((++_sp & 255u) == 0u) { if (xb_ld(&(bar)[XB_TMO])) break; if (_sp > XB_SPIN_CAP) { atomicAdd(&(bar)[XB_TMO], 1u); break; } } } } while (0)
; __device__ __forceinline__ void xcd_barrier(const XcdBarrier& b) {
;     ...
;         if (old + 1u == (gen + 1u) * nloc) {
;             __builtin_amdgcn_fence(__ATOMIC_RELEASE, XB_SCOPE);
;             asm volatile("s_waitcnt vmcnt(0)" ::: "memory");
;             const unsigned og = xb_add(&bar[XB_TOP], 1u);
;             const unsigned tg = og / nx;
;             if (og + 1u == (tg + 1u) * nx) xb_add(&bar[XB_TOPGEN], 1u);
;             else XB_SPIN(xb_ld(&bar[XB_TOPGEN]) == tg, bar);
;             __builtin_amdgcn_fence(__ATOMIC_ACQUIRE, XB_SCOPE);
;             xb_add(&bar[XB_XGEN(b.x)], 1u);
.LBB0_428:
	s_andn2_saveexec_b64 s[6:7], s[6:7]
	s_cbranch_execz .LBB0_448
	v_readlane_b32 s8, v255, 40
	s_nop 3
	s_cmp_eq_u32 s8, 1
	s_cbranch_scc0 .Lmy_full_B1
	s_mov_b64 s[4:5], exec
	v_mbcnt_lo_u32_b32 v0, s4, 0
	v_mbcnt_hi_u32_b32 v0, s5, v0
	v_cmp_eq_u32_e32 vcc, 0, v0
	s_waitcnt lgkmcnt(0)
	s_nop 0
	s_branch .Lmy_xg_B1
.Lmy_full_B1:
	s_mov_b64 s[6:7], exec
	buffer_wbl2 sc1
	s_waitcnt lgkmcnt(0)
	s_waitcnt vmcnt(0)
	v_mbcnt_lo_u32_b32 v0, s6, 0
	v_mbcnt_hi_u32_b32 v1, s7, v0
	v_cmp_eq_u32_e32 vcc, 0, v1
	s_and_saveexec_b64 s[8:9], vcc
	s_cbranch_execz .LBB0_431
	s_bcnt1_i32_b64 s6, s[6:7]
	v_mov_b32_e32 v0, s6
	v_mov_b32_e32 v4, 0x7000
	global_atomic_add v4, v4, v0, s[4:5] offset:1024 sc0

; __device__ __forceinline__ unsigned xb_add(unsigned* p, unsigned v) { return __hip_atomic_fetch_add(p, v, __ATOMIC_RELAXED, __HIP_MEMORY_SCOPE_AGENT); }
; __device__ __forceinline__ void xcd_barrier(const XcdBarrier& b) {
;     ...
;         if (old + 1u == (gen + 1u) * nloc) {
;             __builtin_amdgcn_fence(__ATOMIC_RELEASE, XB_SCOPE);
;             asm volatile("s_waitcnt vmcnt(0)" ::: "memory");
;             const unsigned og = xb_add(&bar[XB_TOP], 1u);
.LBB0_810:
	s_andn2_saveexec_b64 s[6:7], s[6:7]
	s_cbranch_execz .LBB0_830
	s_mov_b64 s[6:7], exec
	buffer_wbl2 sc1
	s_waitcnt lgkmcnt(0)
	s_waitcnt vmcnt(0)
	v_mbcnt_lo_u32_b32 v0, s6, 0
	v_mbcnt_hi_u32_b32 v1, s7, v0
	v_cmp_eq_u32_e32 vcc, 0, v1
	s_and_saveexec_b64 s[8:9], vcc
	s_cbranch_execz .LBB0_813
	s_bcnt1_i32_b64 s6, s[6:7]
	v_mov_b32_e32 v0, s6
	v_mov_b32_e32 v4, 0x7000
	global_atomic_add v4, v4, v0, s[4:5] offset:1024 sc0

; #define SEAM() do { if (lo <= ph && ph + 1 < hi) { size_t zb_ = 0; asm volatile("" : "+s"(zb_), "+s"(bar.x)); bar.bar = (unsigned*)(args.ws + WS_CTL + zb_) + CW_BAR; xcd_barrier(bar); } ++ph; } while (0)
; __global__ void __launch_bounds__(NWAVES * 64, 2) mega_fwd(Args args) {
;     ...
;             if (F.wave < 4) { p_scans(F); if (!CV_IN_MIX) p_convert(F, F.l, cv0_, CV_ALL); if (!mixhead_ && F.l + 1 < NLAYER) p_convert(F, F.l + 1, 0, CV_WIN); }
;             else { if (!CV_IN_MIX) p_convert(F, F.l, cv0_, CV_ALL); if (!mixhead_ && F.l + 1 < NLAYER) p_convert(F, F.l + 1, 0, CV_WIN); p_scans(F); } }
;         SEAM();
.LBB0_2163:
	v_readlane_b32 s2, v255, 14
	s_add_i32 s50, s2, 4
	v_readlane_b32 s2, v255, 10
	v_readlane_b32 s3, v255, 11
	s_cmp_lt_i32 s50, s3
	s_cselect_b64 s[2:3], -1, 0
	s_and_b64 s[0:1], s[0:1], s[2:3]
	s_andn2_b64 vcc, exec, s[0:1]
	s_waitcnt vmcnt(0) lgkmcnt(0)
	s_barrier
	s_mov_b64 s[4:5], exec
	v_readlane_b32 s10, v255, 8
	v_readlane_b32 s11, v255, 9
	s_nop 3
	s_and_b64 s[10:11], s[4:5], s[10:11]
	s_mov_b64 exec, s[10:11]
	s_cbranch_execz .Lmy_s4a_done
	buffer_wbl2 sc1
	s_waitcnt vmcnt(0)
	v_readlane_b32 s12, v255, 5
	v_readlane_b32 s13, v255, 6
	s_nop 3
	v_mov_b32_e32 v0, 0xb000
	v_mov_b32_e32 v1, 1
	global_atomic_add v0, v1, s[12:13]
	s_waitcnt vmcnt(0)

; __global__ void __launch_bounds__(NWAVES * 64, 2) mega_fwd(Args args) {
;     ...
;                 for (;;) {
;                     if (F.tid == 0) QS[0] = (int)__hip_atomic_fetch_add(F.ctl + CW_Q + 64 * F.l + 32, 1u, __ATOMIC_RELAXED, __HIP_MEMORY_SCOPE_AGENT);
;                     __syncthreads();
;                     const int j = __builtin_amdgcn_readfirstlane(QS[0]);
;                     __syncthreads();
;                     if (j >= (QMODE == 4 ? 512 : 1024)) break;
;                     if (QMODE == 3) { SgPre P_; sg_load(F, j >> 2, j & 3, P_); sg_unit(F, F.l, j >> 2, j & 3, P_); } else if (QMODE == 4) ssd_out_unit(F, F.l, j >> 1, j & 1); else { MlPre P_; ml_out_load(F, j >> 2, j & 3, P_); ml_out_unit(F, F.l, j >> 2, j & 3, P_); }
.LBB0_2845:
	s_mov_b64 s[26:27], exec
	v_cmp_eq_u32_e32 vcc, 0, v130
	s_and_b64 exec, exec, vcc
	s_cbranch_execz .Lmy_s4w_done
	s_add_u32 s0, s10, s12
	s_addc_u32 s1, s11, s13
	s_add_u32 s24, s0, 0x9080
	s_addc_u32 s25, s1, 0
	v_mov_b32_e32 v247, 1
	global_atomic_add v246, v3, v247, s[24:25] sc0
	s_add_u32 s28, s10, 0xb000
	s_addc_u32 s29, s11, 0
	s_add_i32 s30, s8, 1
	s_lshl_b32 s30, s30, 8
	s_mov_b32 s32, 0
	v_mov_b32_e32 v0, 0
	buffer_inv sc1

; __device__ __forceinline__ unsigned xb_add(unsigned* p, unsigned v) { return __hip_atomic_fetch_add(p, v, __ATOMIC_RELAXED, __HIP_MEMORY_SCOPE_AGENT); }
; __device__ __forceinline__ void xcd_barrier(const XcdBarrier& b) {
;     ...
;         __builtin_amdgcn_s_waitcnt(0);
;         unsigned nloc = b.st[0], nx = b.st[1];
;         if (nloc == 0u) { xcd_barrier_complete(bar, b.x, nloc, nx); b.st[0] = nloc; b.st[1] = nx; }
;         const unsigned old = xb_add(&bar[XB_XSUB(b.x)], 1u);
;         const unsigned gen = old / nloc;
.LBB0_3895:
	s_mov_b64 s[4:5], exec
	v_mbcnt_lo_u32_b32 v0, s4, 0
	s_add_u32 s22, s2, 0x4000
	v_readlane_b32 s6, v255, 7
	v_mbcnt_hi_u32_b32 v1, s5, v0
	s_addc_u32 s23, s3, 0
	s_lshl_b32 s24, s6, 6
	v_cmp_eq_u32_e32 vcc, 0, v1
	s_and_saveexec_b64 s[6:7], vcc
	s_cbranch_execz .LBB0_3897
	s_add_i32 s52, s24, 0x500
	s_lshl_b64 s[8:9], s[52:53], 2
	s_add_u32 s8, s22, s8
	s_addc_u32 s9, s23, s9
	s_bcnt1_i32_b64 s4, s[4:5]
	v_mov_b32_e32 v0, s4
	global_atomic_add v5, v3, v0, s[8:9] sc0
	buffer_inv sc1

; __device__ __forceinline__ unsigned xb_add(unsigned* p, unsigned v) { return __hip_atomic_fetch_add(p, v, __ATOMIC_RELAXED, __HIP_MEMORY_SCOPE_AGENT); }
; __device__ __forceinline__ void xcd_barrier(const XcdBarrier& b) {
;     ...
;         if (old + 1u == (gen + 1u) * nloc) {
;             __builtin_amdgcn_fence(__ATOMIC_RELEASE, XB_SCOPE);
;             asm volatile("s_waitcnt vmcnt(0)" ::: "memory");
;             const unsigned og = xb_add(&bar[XB_TOP], 1u);
.LBB0_3912:
	s_mov_b64 s[4:5], exec
	buffer_wbl2 sc1
	s_waitcnt lgkmcnt(0)
	s_waitcnt vmcnt(0)
	v_mbcnt_lo_u32_b32 v0, s4, 0
	v_mbcnt_hi_u32_b32 v1, s5, v0
	v_cmp_eq_u32_e32 vcc, 0, v1
	s_and_saveexec_b64 s[6:7], vcc
	s_cbranch_execz .LBB0_3914
	s_bcnt1_i32_b64 s4, s[4:5]
	v_mov_b32_e32 v0, s4
	v_mov_b32_e32 v4, 0x7000
	global_atomic_add v4, v4, v0, s[2:3] offset:1024 sc0
